# v22b: v21 + MLA softmax packed-f32 FMAs (step 1 and 2) and packed row-sum adds (step 1)
# baseline (speedup 1.0000x reference)
.LBB0_946:
	s_sub_i32 s1, s37, 94
	s_cmp_gt_i32 s1, s35
	s_cbranch_scc1 .Lmla_qkskip1
	s_mov_b32 s98, 0x3dd53b94
	s_lshl_b32 s50, s0, 14
	s_add_i32 s1, s50, 0
	v_add_u32_e32 v210, s1, v202
	ds_read_b128 v[98:101], v210 offset:49152
	ds_read_b128 v[102:105], v210 offset:57344
	v_xor_b32_e32 v210, 0x80, v210
	v_max_f32_e32 v186, v67, v67
	v_max_f32_e32 v187, v66, v66
	v_max_f32_e32 v186, v187, v186
	s_waitcnt lgkmcnt(1)
	v_mfma_f32_32x32x16_bf16 v[114:129], v[98:101], v[130:133], 0
	v_add_u32_e32 v212, s1, v207
	v_max3_f32 v186, v186, v68, v69
	ds_read_b128 v[178:181], v212 offset:49152
	ds_read_b128 v[182:185], v212 offset:57344
	v_xor_b32_e32 v212, 0x80, v212
	v_max3_f32 v186, v186, v70, v71
	v_max3_f32 v186, v186, v72, v73
	v_max3_f32 v186, v186, v74, v75
	v_max3_f32 v186, v186, v76, v77
	s_waitcnt lgkmcnt(2)
	v_mfma_f32_32x32x16_bf16 v[98:113], v[102:105], v[130:133], 0
	v_max3_f32 v186, v186, v78, v79
	v_lshl_add_u32 v211, s0, 13, v225
	v_max3_f32 v213, v186, v80, v81
	s_waitcnt lgkmcnt(1)
	v_mfma_f32_32x32x16_bf16 v[114:129], v[178:181], v[134:137], v[114:129]
	v_max3_f32 v178, v213, v82, v83
	v_max3_f32 v178, v178, v84, v85
	v_max3_f32 v178, v178, v86, v87
	v_max3_f32 v178, v178, v88, v89
	v_max3_f32 v178, v178, v90, v91
	v_max3_f32 v178, v178, v92, v93
	v_max3_f32 v178, v178, v94, v95
	v_max3_f32 v178, v178, v96, v97
	v_mov_b32_e32 v179, v178
	s_nop 1
	v_permlane32_swap_b32_e32 v178, v179
	v_max_f32_e32 v179, v179, v179
	v_max_f32_e32 v178, v178, v178
	v_max_f32_e32 v178, v178, v179
	v_sub_f32_e32 v179, v178, v231
	v_mul_f32_e32 v179, 0x3d93cd3a, v179
	v_cmp_ge_f32_e32 vcc, s36, v179
	s_cmp_eq_u64 vcc, exec
	v_max_f32_e32 v179, v231, v231
	s_waitcnt lgkmcnt(0)
	v_mfma_f32_32x32x16_bf16 v[98:113], v[182:185], v[134:137], v[98:113]
	s_cselect_b64 vcc, -1, 0
	v_max_f32_e32 v178, v179, v178
	v_cndmask_b32_e32 v232, v178, v231, vcc
	v_add_u32_e32 v218, s1, v209
	v_sub_f32_e32 v178, v231, v232
	ds_read_b128 v[186:189], v218 offset:49152
	ds_read_b128 v[190:193], v218 offset:57344
	v_xor_b32_e32 v218, 0x80, v218
	v_mul_f32_e32 v178, 0x3dd53b94, v178
	v_exp_f32_e32 v231, v178
	v_mul_f32_e32 v213, 0xbdd53b94, v232
	v_pk_fma_f32 v[66:67], v[66:67], s[98:99], v[212:213] op_sel:[0,0,1] op_sel_hi:[1,0,1]
	s_waitcnt lgkmcnt(1)
	v_mfma_f32_32x32x16_bf16 v[114:129], v[186:189], v[138:141], v[114:129]
	v_exp_f32_e32 v66, v66
	v_pk_fma_f32 v[82:83], v[82:83], s[98:99], v[212:213] op_sel:[0,0,1] op_sel_hi:[1,0,1]
	v_add_u32_e32 v219, s1, v224
	v_exp_f32_e32 v82, v82
	ds_read_b128 v[178:181], v219 offset:49152
	ds_read_b128 v[182:185], v219 offset:57344
	v_xor_b32_e32 v219, 0x80, v219
	v_exp_f32_e32 v67, v67
	s_waitcnt lgkmcnt(2)
	v_mfma_f32_32x32x16_bf16 v[98:113], v[190:193], v[138:141], v[98:113]
	v_exp_f32_e32 v83, v83
	s_nop 0
	v_pk_add_f32 v[220:221], v[66:67], v[82:83]
	v_pk_fma_f32 v[68:69], v[68:69], s[98:99], v[212:213] op_sel:[0,0,1] op_sel_hi:[1,0,1]
	s_waitcnt lgkmcnt(1)
	v_mfma_f32_32x32x16_bf16 v[114:129], v[178:181], v[142:145], v[114:129]
	v_exp_f32_e32 v68, v68
	v_pk_fma_f32 v[84:85], v[84:85], s[98:99], v[212:213] op_sel:[0,0,1] op_sel_hi:[1,0,1]
	v_exp_f32_e32 v84, v84
	ds_read_b128 v[186:189], v210 offset:49152
	ds_read_b128 v[190:193], v210 offset:57344
	v_exp_f32_e32 v69, v69
	s_waitcnt lgkmcnt(2)
	v_mfma_f32_32x32x16_bf16 v[98:113], v[182:185], v[142:145], v[98:113]
	v_exp_f32_e32 v85, v85
	v_pk_add_f32 v[220:221], v[220:221], v[68:69]
	v_pk_add_f32 v[220:221], v[220:221], v[84:85]
	v_pk_fma_f32 v[70:71], v[70:71], s[98:99], v[212:213] op_sel:[0,0,1] op_sel_hi:[1,0,1]
	s_waitcnt lgkmcnt(1)
	v_mfma_f32_32x32x16_bf16 v[114:129], v[186:189], v[146:149], v[114:129]
	v_exp_f32_e32 v70, v70
	v_pk_fma_f32 v[86:87], v[86:87], s[98:99], v[212:213] op_sel:[0,0,1] op_sel_hi:[1,0,1]
	v_exp_f32_e32 v86, v86
	ds_read_b128 v[178:181], v212 offset:49152
	ds_read_b128 v[182:185], v212 offset:57344
	v_exp_f32_e32 v71, v71
	s_waitcnt lgkmcnt(2)
	v_mfma_f32_32x32x16_bf16 v[98:113], v[190:193], v[146:149], v[98:113]
	v_exp_f32_e32 v87, v87
	v_pk_add_f32 v[220:221], v[220:221], v[70:71]
	v_pk_add_f32 v[220:221], v[220:221], v[86:87]
	v_pk_fma_f32 v[72:73], v[72:73], s[98:99], v[212:213] op_sel:[0,0,1] op_sel_hi:[1,0,1]
	s_waitcnt lgkmcnt(1)
	v_mfma_f32_32x32x16_bf16 v[114:129], v[178:181], v[150:153], v[114:129]
	v_exp_f32_e32 v72, v72
	v_pk_fma_f32 v[88:89], v[88:89], s[98:99], v[212:213] op_sel:[0,0,1] op_sel_hi:[1,0,1]
	v_exp_f32_e32 v88, v88
	ds_read_b128 v[186:189], v218 offset:49152
	ds_read_b128 v[190:193], v218 offset:57344
	v_exp_f32_e32 v73, v73
	s_waitcnt lgkmcnt(2)
	v_mfma_f32_32x32x16_bf16 v[98:113], v[182:185], v[150:153], v[98:113]
	v_exp_f32_e32 v89, v89
	v_pk_add_f32 v[220:221], v[220:221], v[72:73]
	v_pk_add_f32 v[220:221], v[220:221], v[88:89]
	v_pk_fma_f32 v[74:75], v[74:75], s[98:99], v[212:213] op_sel:[0,0,1] op_sel_hi:[1,0,1]
	v_exp_f32_e32 v74, v74
	v_pk_fma_f32 v[90:91], v[90:91], s[98:99], v[212:213] op_sel:[0,0,1] op_sel_hi:[1,0,1]
	s_waitcnt lgkmcnt(1)
	v_mfma_f32_32x32x16_bf16 v[114:129], v[186:189], v[154:157], v[114:129]
	v_exp_f32_e32 v90, v90
	v_exp_f32_e32 v75, v75
	ds_read_b128 v[178:181], v219 offset:49152
	ds_read_b128 v[182:185], v219 offset:57344
	v_exp_f32_e32 v91, v91
	s_waitcnt lgkmcnt(2)
	v_mfma_f32_32x32x16_bf16 v[98:113], v[190:193], v[154:157], v[98:113]
	v_pk_add_f32 v[220:221], v[220:221], v[74:75]
	v_pk_add_f32 v[220:221], v[220:221], v[90:91]
	v_pk_fma_f32 v[76:77], v[76:77], s[98:99], v[212:213] op_sel:[0,0,1] op_sel_hi:[1,0,1]
	v_exp_f32_e32 v76, v76
	v_pk_fma_f32 v[92:93], v[92:93], s[98:99], v[212:213] op_sel:[0,0,1] op_sel_hi:[1,0,1]
	s_waitcnt lgkmcnt(1)
	v_mfma_f32_32x32x16_bf16 v[114:129], v[178:181], v[158:161], v[114:129]
	v_exp_f32_e32 v92, v92
	v_add_u32_e32 v186, v211, v226
	v_exp_f32_e32 v77, v77
	ds_read_b128 v[178:181], v186
	ds_read_b128 v[186:189], v186 offset:4096
	v_exp_f32_e32 v93, v93
	s_waitcnt lgkmcnt(2)
	v_mfma_f32_32x32x16_bf16 v[98:113], v[182:185], v[158:161], v[98:113]
	v_pk_add_f32 v[220:221], v[220:221], v[76:77]
	v_pk_add_f32 v[220:221], v[220:221], v[92:93]
	v_pk_fma_f32 v[78:79], v[78:79], s[98:99], v[212:213] op_sel:[0,0,1] op_sel_hi:[1,0,1]
	v_exp_f32_e32 v78, v78
	v_pk_fma_f32 v[94:95], v[94:95], s[98:99], v[212:213] op_sel:[0,0,1] op_sel_hi:[1,0,1]
	s_waitcnt lgkmcnt(1)
	v_mfma_f32_32x32x16_bf16 v[114:129], v[178:181], v[162:165], v[114:129]
	v_exp_f32_e32 v94, v94
	v_add_u32_e32 v182, v211, v206
	v_exp_f32_e32 v79, v79
	ds_read_b128 v[178:181], v182
	ds_read_b128 v[182:185], v182 offset:4096
	v_exp_f32_e32 v95, v95
	s_waitcnt lgkmcnt(2)
	v_mfma_f32_32x32x16_bf16 v[98:113], v[186:189], v[162:165], v[98:113]
	v_pk_add_f32 v[220:221], v[220:221], v[78:79]
	v_pk_add_f32 v[220:221], v[220:221], v[94:95]
	v_pk_fma_f32 v[80:81], v[80:81], s[98:99], v[212:213] op_sel:[0,0,1] op_sel_hi:[1,0,1]
	v_exp_f32_e32 v80, v80
	v_pk_fma_f32 v[96:97], v[96:97], s[98:99], v[212:213] op_sel:[0,0,1] op_sel_hi:[1,0,1]
	s_waitcnt lgkmcnt(1)
	v_mfma_f32_32x32x16_bf16 v[114:129], v[178:181], v[166:169], v[114:129]
	v_exp_f32_e32 v96, v96
	v_add_u32_e32 v186, v211, v208
	v_exp_f32_e32 v81, v81
	ds_read_b128 v[178:181], v186
	ds_read_b128 v[186:189], v186 offset:4096
	v_exp_f32_e32 v97, v97
	s_waitcnt lgkmcnt(2)
	v_mfma_f32_32x32x16_bf16 v[98:113], v[182:185], v[166:169], v[98:113]
	v_pk_add_f32 v[220:221], v[220:221], v[80:81]
	v_pk_add_f32 v[220:221], v[220:221], v[96:97]
	v_add_f32_e32 v233, v220, v221
	s_waitcnt lgkmcnt(1)
	v_mfma_f32_32x32x16_bf16 v[114:129], v[178:181], v[170:173], v[114:129]
	v_add_u32_e32 v182, v211, v223
	ds_read_b128 v[190:193], v182
	ds_read_b128 v[236:239], v182 offset:4096
	v_mov_b32_e32 v234, v233
	v_cvt_pk_bf16_f32 v178, v66, v67
	v_cvt_pk_bf16_f32 v179, v68, v69
	v_cvt_pk_bf16_f32 v180, v70, v71
	v_cvt_pk_bf16_f32 v181, v72, v73
	s_waitcnt lgkmcnt(2)
	v_mfma_f32_32x32x16_bf16 v[98:113], v[186:189], v[170:173], v[98:113]
	v_cvt_pk_bf16_f32 v182, v74, v75
	v_cvt_pk_bf16_f32 v183, v76, v77
	v_cvt_pk_bf16_f32 v184, v78, v79
	v_cvt_pk_bf16_f32 v185, v80, v81
	v_permlane32_swap_b32_e32 v233, v234
	v_permlane32_swap_b32_e32 v178, v180
	v_permlane32_swap_b32_e32 v179, v181
	v_permlane32_swap_b32_e32 v182, v184
	v_permlane32_swap_b32_e32 v183, v185
	s_waitcnt lgkmcnt(1)
	v_mfma_f32_32x32x16_bf16 v[114:129], v[190:193], v[174:177], v[114:129]
	v_cvt_pk_bf16_f32 v186, v82, v83
	v_cvt_pk_bf16_f32 v187, v84, v85
	v_cvt_pk_bf16_f32 v188, v86, v87
	v_cvt_pk_bf16_f32 v189, v88, v89
	v_cvt_pk_bf16_f32 v190, v90, v91
	v_cvt_pk_bf16_f32 v191, v92, v93
	v_cvt_pk_bf16_f32 v192, v94, v95
	s_waitcnt lgkmcnt(0)
	v_mfma_f32_32x32x16_bf16 v[98:113], v[236:239], v[174:177], v[98:113]
	v_cvt_pk_bf16_f32 v193, v96, v97
	v_permlane32_swap_b32_e32 v186, v188
	v_permlane32_swap_b32_e32 v187, v189
	v_permlane32_swap_b32_e32 v190, v192
	v_permlane32_swap_b32_e32 v191, v193

.LBB0_958:
	s_mov_b32 s98, 0x3dd53b94
	s_lshl_b32 s0, s48, 14
	s_add_i32 s0, s0, 0
	v_add_u32_e32 v210, s0, v202
	ds_read_b128 v[66:69], v210 offset:49152
	ds_read_b128 v[82:85], v210 offset:57344
	v_xor_b32_e32 v210, 0x80, v210
	v_max_f32_e32 v86, v237, v236
	v_max3_f32 v86, v86, v116, v117
	v_max3_f32 v86, v86, v118, v119
	v_max3_f32 v186, v86, v120, v121
	v_add_u32_e32 v212, s0, v207
	ds_read_b128 v[178:181], v212 offset:49152
	ds_read_b128 v[182:185], v212 offset:57344
	v_xor_b32_e32 v212, 0x80, v212
	v_max3_f32 v186, v186, v122, v123
	s_waitcnt lgkmcnt(3)
	v_mfma_f32_32x32x16_bf16 v[66:81], v[66:69], v[130:133], 0
	v_max3_f32 v186, v186, v124, v125
	v_max3_f32 v186, v186, v126, v127
	v_lshl_add_u32 v211, s48, 13, v225
	v_max3_f32 v213, v186, v128, v129
	s_waitcnt lgkmcnt(2)
	v_mfma_f32_32x32x16_bf16 v[82:97], v[82:85], v[130:133], 0
	s_waitcnt lgkmcnt(1)
	v_mfma_f32_32x32x16_bf16 v[66:81], v[178:181], v[134:137], v[66:81]
	v_max3_f32 v178, v213, v98, v99
	v_max3_f32 v178, v178, v100, v101
	v_max3_f32 v178, v178, v102, v103
	v_max3_f32 v178, v178, v104, v105
	v_max3_f32 v178, v178, v106, v107
	v_max3_f32 v178, v178, v108, v109
	v_max3_f32 v178, v178, v110, v111
	v_max3_f32 v178, v178, v112, v113
	v_mov_b32_e32 v179, v178
	s_nop 1
	v_permlane32_swap_b32_e32 v178, v179
	v_max_f32_e32 v179, v179, v179
	v_max_f32_e32 v178, v178, v178
	v_max_f32_e32 v178, v178, v179
	v_sub_f32_e32 v179, v178, v232
	v_mul_f32_e32 v179, 0x3d93cd3a, v179
	v_cmp_ge_f32_e32 vcc, s36, v179
	s_cmp_eq_u64 vcc, exec
	s_waitcnt lgkmcnt(0)
	v_mfma_f32_32x32x16_bf16 v[82:97], v[182:185], v[134:137], v[82:97]
	s_cselect_b64 vcc, -1, 0
	v_max_f32_e32 v178, v235, v178
	v_cndmask_b32_e32 v231, v178, v232, vcc
	v_add_u32_e32 v218, s0, v209
	v_sub_f32_e32 v178, v232, v231
	ds_read_b128 v[186:189], v218 offset:49152
	ds_read_b128 v[190:193], v218 offset:57344
	v_xor_b32_e32 v218, 0x80, v218
	v_mul_f32_e32 v178, 0x3dd53b94, v178
	v_exp_f32_e32 v234, v178
	v_mul_f32_e32 v213, 0xbdd53b94, v231
	v_pk_fma_f32 v[114:115], v[114:115], s[98:99], v[212:213] op_sel:[0,0,1] op_sel_hi:[1,0,1]
	s_waitcnt lgkmcnt(1)
	v_mfma_f32_32x32x16_bf16 v[66:81], v[186:189], v[138:141], v[66:81]
	v_exp_f32_e32 v220, v114
	v_pk_fma_f32 v[98:99], v[98:99], s[98:99], v[212:213] op_sel:[0,0,1] op_sel_hi:[1,0,1]
	v_add_u32_e32 v219, s0, v224
	v_exp_f32_e32 v221, v98
	ds_read_b128 v[178:181], v219 offset:49152
	ds_read_b128 v[182:185], v219 offset:57344
	v_xor_b32_e32 v219, 0x80, v219
	v_exp_f32_e32 v232, v115
	s_waitcnt lgkmcnt(2)
	v_mfma_f32_32x32x16_bf16 v[82:97], v[190:193], v[138:141], v[82:97]
	v_exp_f32_e32 v235, v99
	v_add_f32_e32 v98, 0, v220
	v_add_f32_e32 v98, v221, v98
	v_add_f32_e32 v98, v232, v98
	v_add_f32_e32 v98, v235, v98
	v_pk_fma_f32 v[116:117], v[116:117], s[98:99], v[212:213] op_sel:[0,0,1] op_sel_hi:[1,0,1]
	ds_read_b128 v[186:189], v210 offset:49152
	ds_read_b128 v[190:193], v210 offset:57344
	v_exp_f32_e32 v210, v116
	v_pk_fma_f32 v[100:101], v[100:101], s[98:99], v[212:213] op_sel:[0,0,1] op_sel_hi:[1,0,1]
	s_waitcnt lgkmcnt(3)
	v_mfma_f32_32x32x16_bf16 v[66:81], v[178:181], v[142:145], v[66:81]
	v_exp_f32_e32 v236, v100
	v_exp_f32_e32 v237, v117
	v_exp_f32_e32 v238, v101
	v_add_f32_e32 v98, v210, v98
	v_add_f32_e32 v98, v236, v98
	s_waitcnt lgkmcnt(2)
	v_mfma_f32_32x32x16_bf16 v[82:97], v[182:185], v[142:145], v[82:97]
	v_add_f32_e32 v98, v237, v98
	v_add_f32_e32 v178, v238, v98
	v_pk_fma_f32 v[118:119], v[118:119], s[98:99], v[212:213] op_sel:[0,0,1] op_sel_hi:[1,0,1]
	s_waitcnt lgkmcnt(1)
	v_mfma_f32_32x32x16_bf16 v[66:81], v[186:189], v[146:149], v[66:81]
	v_exp_f32_e32 v118, v118
	v_pk_fma_f32 v[102:103], v[102:103], s[98:99], v[212:213] op_sel:[0,0,1] op_sel_hi:[1,0,1]
	ds_read_b128 v[98:101], v212 offset:49152
	ds_read_b128 v[114:117], v212 offset:57344
	v_exp_f32_e32 v212, v102
	v_exp_f32_e32 v119, v119
	s_waitcnt lgkmcnt(2)
	v_mfma_f32_32x32x16_bf16 v[82:97], v[190:193], v[146:149], v[82:97]
	v_exp_f32_e32 v188, v103
	v_add_f32_e32 v102, v118, v178
	v_add_f32_e32 v102, v212, v102
	v_add_f32_e32 v102, v119, v102
	v_add_f32_e32 v102, v188, v102
	v_pk_fma_f32 v[120:121], v[120:121], s[98:99], v[212:213] op_sel:[0,0,1] op_sel_hi:[1,0,1]
	s_waitcnt lgkmcnt(1)
	v_mfma_f32_32x32x16_bf16 v[66:81], v[98:101], v[150:153], v[66:81]
	v_exp_f32_e32 v120, v120
	v_pk_fma_f32 v[104:105], v[104:105], s[98:99], v[212:213] op_sel:[0,0,1] op_sel_hi:[1,0,1]
	v_exp_f32_e32 v189, v104
	ds_read_b128 v[178:181], v218 offset:49152
	ds_read_b128 v[182:185], v218 offset:57344
	v_exp_f32_e32 v121, v121
	s_waitcnt lgkmcnt(2)
	v_mfma_f32_32x32x16_bf16 v[82:97], v[114:117], v[150:153], v[82:97]
	v_exp_f32_e32 v190, v105
	v_add_f32_e32 v98, v120, v102
	v_add_f32_e32 v98, v189, v98
	v_add_f32_e32 v98, v121, v98
	v_add_f32_e32 v114, v190, v98
	v_pk_fma_f32 v[122:123], v[122:123], s[98:99], v[212:213] op_sel:[0,0,1] op_sel_hi:[1,0,1]
	v_exp_f32_e32 v122, v122
	s_waitcnt lgkmcnt(1)
	v_mfma_f32_32x32x16_bf16 v[66:81], v[178:181], v[154:157], v[66:81]
	v_pk_fma_f32 v[106:107], v[106:107], s[98:99], v[212:213] op_sel:[0,0,1] op_sel_hi:[1,0,1]
	v_exp_f32_e32 v191, v106
	v_add_f32_e32 v106, v122, v114
	ds_read_b128 v[98:101], v219 offset:49152
	ds_read_b128 v[102:105], v219 offset:57344
	v_exp_f32_e32 v123, v123
	s_waitcnt lgkmcnt(2)
	v_mfma_f32_32x32x16_bf16 v[82:97], v[182:185], v[154:157], v[82:97]
	v_exp_f32_e32 v192, v107
	v_add_f32_e32 v106, v191, v106
	v_add_f32_e32 v106, v123, v106
	v_add_f32_e32 v106, v192, v106
	v_pk_fma_f32 v[124:125], v[124:125], s[98:99], v[212:213] op_sel:[0,0,1] op_sel_hi:[1,0,1]
	s_waitcnt lgkmcnt(1)
	v_mfma_f32_32x32x16_bf16 v[66:81], v[98:101], v[158:161], v[66:81]
	v_add_u32_e32 v107, v211, v226
	v_exp_f32_e32 v124, v124
	v_pk_fma_f32 v[108:109], v[108:109], s[98:99], v[212:213] op_sel:[0,0,1] op_sel_hi:[1,0,1]
	v_exp_f32_e32 v193, v108
	ds_read_b128 v[98:101], v107
	ds_read_b128 v[114:117], v107 offset:4096
	v_exp_f32_e32 v125, v125
	s_waitcnt lgkmcnt(2)
	v_mfma_f32_32x32x16_bf16 v[82:97], v[102:105], v[158:161], v[82:97]
	v_exp_f32_e32 v218, v109
	v_add_f32_e32 v106, v124, v106
	v_add_f32_e32 v106, v193, v106
	v_add_f32_e32 v102, v125, v106
	v_add_f32_e32 v106, v218, v102
	v_pk_fma_f32 v[126:127], v[126:127], s[98:99], v[212:213] op_sel:[0,0,1] op_sel_hi:[1,0,1]
	s_waitcnt lgkmcnt(1)
	v_mfma_f32_32x32x16_bf16 v[66:81], v[98:101], v[162:165], v[66:81]
	v_exp_f32_e32 v126, v126
	v_pk_fma_f32 v[110:111], v[110:111], s[98:99], v[212:213] op_sel:[0,0,1] op_sel_hi:[1,0,1]
	v_add_u32_e32 v102, v211, v206
	v_exp_f32_e32 v219, v110
	ds_read_b128 v[98:101], v102
	ds_read_b128 v[102:105], v102 offset:4096
	v_exp_f32_e32 v127, v127
	s_waitcnt lgkmcnt(2)
	v_mfma_f32_32x32x16_bf16 v[82:97], v[114:117], v[162:165], v[82:97]
	v_exp_f32_e32 v239, v111
	v_add_f32_e32 v106, v126, v106
	v_add_f32_e32 v106, v219, v106
	v_add_f32_e32 v106, v127, v106
	v_add_f32_e32 v110, v239, v106
	v_pk_fma_f32 v[128:129], v[128:129], s[98:99], v[212:213] op_sel:[0,0,1] op_sel_hi:[1,0,1]
	s_waitcnt lgkmcnt(1)
	v_mfma_f32_32x32x16_bf16 v[66:81], v[98:101], v[166:169], v[66:81]
	v_exp_f32_e32 v114, v128
	v_pk_fma_f32 v[112:113], v[112:113], s[98:99], v[212:213] op_sel:[0,0,1] op_sel_hi:[1,0,1]
	v_add_u32_e32 v106, v211, v208
	v_exp_f32_e32 v115, v112
	ds_read_b128 v[98:101], v106
	ds_read_b128 v[106:109], v106 offset:4096
	v_exp_f32_e32 v116, v129
	s_waitcnt lgkmcnt(2)
	v_mfma_f32_32x32x16_bf16 v[82:97], v[102:105], v[166:169], v[82:97]
	v_exp_f32_e32 v117, v113
	v_add_f32_e32 v110, v114, v110
	v_add_f32_e32 v110, v115, v110
	v_add_f32_e32 v102, v116, v110
	v_add_f32_e32 v128, v117, v102
	s_waitcnt lgkmcnt(1)
	v_mfma_f32_32x32x16_bf16 v[66:81], v[98:101], v[170:173], v[66:81]
	v_add_u32_e32 v110, v211, v223
	ds_read_b128 v[102:105], v110
	ds_read_b128 v[110:113], v110 offset:4096
	v_mov_b32_e32 v129, v128
	s_nop 1
	v_permlane32_swap_b32_e32 v128, v129
	v_add_f32_e32 v230, v128, v129
	v_cvt_pk_bf16_f32 v178, v220, v232
	s_waitcnt lgkmcnt(2)
	v_mfma_f32_32x32x16_bf16 v[82:97], v[106:109], v[170:173], v[82:97]
	v_cvt_pk_bf16_f32 v179, v210, v237
	v_cvt_pk_bf16_f32 v180, v118, v119
	v_cvt_pk_bf16_f32 v181, v120, v121
	v_cvt_pk_bf16_f32 v182, v122, v123
	v_cvt_pk_bf16_f32 v183, v124, v125
	v_cvt_pk_bf16_f32 v184, v126, v127
	v_cvt_pk_bf16_f32 v185, v114, v116
	v_fmac_f32_e32 v230, v233, v234
	v_permlane32_swap_b32_e32 v178, v180
	v_permlane32_swap_b32_e32 v179, v181
	v_permlane32_swap_b32_e32 v182, v184
	v_permlane32_swap_b32_e32 v183, v185
	s_waitcnt lgkmcnt(1)
	v_mfma_f32_32x32x16_bf16 v[66:81], v[102:105], v[174:177], v[66:81]
	v_cvt_pk_bf16_f32 v186, v221, v235
	v_cvt_pk_bf16_f32 v187, v236, v238
	v_cvt_pk_bf16_f32 v188, v212, v188
	v_cvt_pk_bf16_f32 v189, v189, v190
	v_cvt_pk_bf16_f32 v190, v191, v192
	v_cvt_pk_bf16_f32 v191, v193, v218
	v_cvt_pk_bf16_f32 v192, v219, v239
	s_waitcnt lgkmcnt(0)
	v_mfma_f32_32x32x16_bf16 v[82:97], v[110:113], v[174:177], v[82:97]
	v_cvt_pk_bf16_f32 v193, v115, v117
	v_permlane32_swap_b32_e32 v186, v188
	v_permlane32_swap_b32_e32 v187, v189
	v_permlane32_swap_b32_e32 v190, v192
	v_permlane32_swap_b32_e32 v191, v193
	v_cmp_gt_f32_e32 vcc, 1.0, v234
	s_cbranch_vccz .LBB0_962
